# P4 decay/iclr loads and all P6 loads (once-read) with nt policy
# baseline (speedup 1.0000x reference)
; __device__ __forceinline__ void p4_rwkv_prep(Frame& F) {
;     ...
;         for (int k = 0; k < 4; ++k) { const int t = tb + k * tstep; const v2u z0 = {0u, 0u};
;             zcr[k] = zck[k] = zcv[k] = zpr[k] = zpk[k] = zpv[k] = ic[k] = z0; wd[k] = (f32x4){0.f, 0.f, 0.f, 0.f};
;             if (t < S_) { const bf16* zc = ZR + (size_t)t * ZR_LD + c;
;                 zcr[k] = *(const v2u*)zc; zck[k] = *(const v2u*)(zc + 2048); zcv[k] = *(const v2u*)(zc + 4096);
;                 if (t > 0) { const bf16* zp = zc - ZR_LD; zpr[k] = *(const v2u*)zp; zpk[k] = *(const v2u*)(zp + 2048); zpv[k] = *(const v2u*)(zp + 4096); }
;                 ic[k] = *(const v2u*)(ICLR + (size_t)t * RW + c); wd[k] = *(const f32x4*)(WDEC + (size_t)t * RW + c); } }
.LBB0_1851:
	v_lshl_add_u64 v[26:27], s[68:69], 0, v[64:65]
	v_lshl_add_u64 v[28:29], s[68:69], 0, v[66:67]
	global_load_dwordx2 v[110:111], v[26:27], off nt
	global_load_dwordx4 v[38:41], v[28:29], off nt
	s_add_i32 s50, s76, s6
	s_cmpk_lt_i32 s50, 0x2000
	s_cselect_b64 s[54:55], -1, 0
	s_cmpk_gt_i32 s50, 0x1fff
	s_cbranch_scc1 .LBB0_1854
	v_mad_i64_i32 v[26:27], s[44:45], s50, v125, v[42:43]
	v_add_co_u32_e32 v28, vcc, 0x1000, v26
	s_cmp_lt_i32 s50, 1
	s_nop 0
	v_addc_co_u32_e32 v29, vcc, 0, v27, vcc
	v_add_co_u32_e32 v30, vcc, 0x2000, v26
	s_nop 1
	v_addc_co_u32_e32 v31, vcc, 0, v27, vcc
	global_load_dwordx2 v[98:99], v[26:27], off
	global_load_dwordx2 v[100:101], v[28:29], off
	global_load_dwordx2 v[102:103], v[30:31], off
	s_cbranch_scc1 .LBB0_1855
	v_add_co_u32_e32 v28, vcc, 0xffffd000, v26
	s_nop 1
	v_addc_co_u32_e32 v29, vcc, -1, v27, vcc
	v_add_co_u32_e32 v30, vcc, 0xffffe000, v26
	s_nop 1
	v_addc_co_u32_e32 v31, vcc, -1, v27, vcc
	v_add_co_u32_e32 v26, vcc, 0xfffff000, v26
	s_nop 1
	v_addc_co_u32_e32 v27, vcc, -1, v27, vcc
	global_load_dwordx2 v[104:105], v[28:29], off offset:-1024
	global_load_dwordx2 v[106:107], v[30:31], off offset:-1024
	global_load_dwordx2 v[108:109], v[26:27], off offset:-1024
	s_branch .LBB0_1856

; __device__ __forceinline__ void p4_rwkv_prep(Frame& F) {
;     ...
;         for (int k = 0; k < 4; ++k) { const int t = tb + k * tstep; const v2u z0 = {0u, 0u};
;             zcr[k] = zck[k] = zcv[k] = zpr[k] = zpk[k] = zpv[k] = ic[k] = z0; wd[k] = (f32x4){0.f, 0.f, 0.f, 0.f};
;             if (t < S_) { const bf16* zc = ZR + (size_t)t * ZR_LD + c;
;                 zcr[k] = *(const v2u*)zc; zck[k] = *(const v2u*)(zc + 2048); zcv[k] = *(const v2u*)(zc + 4096);
;                 if (t > 0) { const bf16* zp = zc - ZR_LD; zpr[k] = *(const v2u*)zp; zpk[k] = *(const v2u*)(zp + 2048); zpv[k] = *(const v2u*)(zp + 4096); }
;                 ic[k] = *(const v2u*)(ICLR + (size_t)t * RW + c); wd[k] = *(const f32x4*)(WDEC + (size_t)t * RW + c); } }
.LBB0_1856:
	s_ashr_i32 s51, s50, 31
	s_lshl_b64 s[44:45], s[50:51], 12
	v_lshl_add_u64 v[26:27], v[44:45], 0, s[44:45]
	s_lshl_b64 s[44:45], s[50:51], 13
	v_lshl_add_u64 v[28:29], v[46:47], 0, s[44:45]
	global_load_dwordx2 v[96:97], v[26:27], off nt
	global_load_dwordx4 v[34:37], v[28:29], off nt

; __device__ __forceinline__ void p4_rwkv_prep(Frame& F) {
;     ...
;         for (int k = 0; k < 4; ++k) { const int t = tb + k * tstep; const v2u z0 = {0u, 0u};
;             zcr[k] = zck[k] = zcv[k] = zpr[k] = zpk[k] = zpv[k] = ic[k] = z0; wd[k] = (f32x4){0.f, 0.f, 0.f, 0.f};
;             if (t < S_) { const bf16* zc = ZR + (size_t)t * ZR_LD + c;
;                 zcr[k] = *(const v2u*)zc; zck[k] = *(const v2u*)(zc + 2048); zcv[k] = *(const v2u*)(zc + 4096);
;                 if (t > 0) { const bf16* zp = zc - ZR_LD; zpr[k] = *(const v2u*)zp; zpk[k] = *(const v2u*)(zp + 2048); zpv[k] = *(const v2u*)(zp + 4096); }
;                 ic[k] = *(const v2u*)(ICLR + (size_t)t * RW + c); wd[k] = *(const f32x4*)(WDEC + (size_t)t * RW + c); } }
.LBB0_1862:
	s_ashr_i32 s47, s46, 31
	s_lshl_b64 s[44:45], s[46:47], 12
	v_lshl_add_u64 v[26:27], v[44:45], 0, s[44:45]
	s_lshl_b64 s[44:45], s[46:47], 13
	v_lshl_add_u64 v[28:29], v[46:47], 0, s[44:45]
	global_load_dwordx2 v[82:83], v[26:27], off nt
	global_load_dwordx4 v[30:33], v[28:29], off nt

; __device__ __forceinline__ void p4_rwkv_prep(Frame& F) {
;     ...
;         for (int k = 0; k < 4; ++k) { const int t = tb + k * tstep; const v2u z0 = {0u, 0u};
;             zcr[k] = zck[k] = zcv[k] = zpr[k] = zpk[k] = zpv[k] = ic[k] = z0; wd[k] = (f32x4){0.f, 0.f, 0.f, 0.f};
;             if (t < S_) { const bf16* zc = ZR + (size_t)t * ZR_LD + c;
;                 zcr[k] = *(const v2u*)zc; zck[k] = *(const v2u*)(zc + 2048); zcv[k] = *(const v2u*)(zc + 4096);
;                 if (t > 0) { const bf16* zp = zc - ZR_LD; zpr[k] = *(const v2u*)zp; zpk[k] = *(const v2u*)(zp + 2048); zpv[k] = *(const v2u*)(zp + 4096); }
;                 ic[k] = *(const v2u*)(ICLR + (size_t)t * RW + c); wd[k] = *(const f32x4*)(WDEC + (size_t)t * RW + c); } }
.LBB0_1869:
	s_ashr_i32 s45, s44, 31
	s_lshl_b64 s[60:61], s[44:45], 12
	v_lshl_add_u64 v[26:27], v[44:45], 0, s[60:61]
	s_lshl_b64 s[60:61], s[44:45], 13
	v_lshl_add_u64 v[28:29], v[46:47], 0, s[60:61]
	global_load_dwordx2 v[68:69], v[26:27], off
	s_nop 0
	global_load_dwordx4 v[26:29], v[28:29], off nt
	s_andn2_b64 vcc, exec, s[4:5]
	s_cbranch_vccnz .LBB0_1867

; __device__ __forceinline__ void p6_rwkv_post(Frame& F) {
;     const float* Y = (const float*)(F.ws + WS_Y); const bf16* GG = (const bf16*)(F.ws + WS_GG); const float* BC = (const float*)(F.ws + WS_BC);
;     const unsigned char* SC = F.ws + WS_SCAN; bf16* YA = (bf16*)(F.ws + WS_YA);
;     const float* gn_w = F.in[12]; const float* gn_b = F.in[13];
;     const int hq = F.gw & 7, c = hq * 256 + 4 * F.lane, h = hq * 4 + (F.lane >> 4), q = F.lane & 15, tstep = F.NGW >> 3;
;     const f32x4 gw4 = *(const f32x4*)(gn_w + c), gb4 = *(const f32x4*)(gn_b + c);
;     for (int tb = F.gw >> 3; tb < S_; tb += 4 * tstep) {
.LBB0_2879:
	s_cmp_gt_i32 s84, 6
	s_cselect_b64 s[0:1], -1, 0
	s_cmp_lt_i32 s85, 7
	s_cselect_b64 s[4:5], -1, 0
	s_or_b64 s[0:1], s[0:1], s[4:5]
	s_and_b64 vcc, exec, s[0:1]
	s_cbranch_vccnz .LBB0_2975
	s_ashr_i32 s4, s94, 3
	s_cmpk_gt_i32 s4, 0x1fff
	v_mbcnt_lo_u32_b32 v1, -1, 0
	v_mbcnt_hi_u32_b32 v1, -1, v1
	s_cbranch_scc1 .LBB0_2896
	s_add_u32 s6, s68, 0x1600000
	s_addc_u32 s7, s69, 0
	s_bfe_u32 s0, s70, 0x30006
	s_lshl_b32 s1, s0, 8
	s_waitcnt vmcnt(1)
	v_lshl_add_u32 v10, v1, 2, s1
	s_waitcnt lgkmcnt(0)
	v_readlane_b32 s8, v254, 2
	s_waitcnt vmcnt(0)
	v_ashrrev_i32_e32 v11, 31, v10
	v_readlane_b32 s9, v254, 3
	v_readlane_b32 s10, v254, 4
	v_readlane_b32 s11, v254, 5
	v_readlane_b32 s16, v254, 10
	v_readlane_b32 s17, v254, 11
	v_lshlrev_b64 v[12:13], 2, v[10:11]
	v_readlane_b32 s18, v254, 12
	v_readlane_b32 s19, v254, 13
	s_mov_b64 s[8:9], s[16:17]
	s_mov_b64 s[10:11], s[18:19]
	v_lshl_add_u64 v[14:15], s[8:9], 0, v[12:13]
	v_lshl_add_u64 v[16:17], s[10:11], 0, v[12:13]
	global_load_dwordx4 v[2:5], v[14:15], off nt
	global_load_dwordx4 v[6:9], v[16:17], off nt
	s_ashr_i32 s38, s34, 2
	v_ashrrev_i32_e32 v18, 4, v1
	s_ashr_i32 s33, s34, 3
	s_add_i32 s5, s4, s38
	v_lshl_add_u32 v45, s4, 5, v18
	v_lshl_add_u32 v57, s5, 5, v18
	s_mul_i32 s5, s33, 0x60
	v_add_u32_e32 v59, s5, v45
	s_add_i32 s5, s4, s33
	s_mov_b64 s[8:9], 0x17000000
	s_ashr_i32 s35, s34, 1
	v_lshl_add_u32 v65, s5, 5, v18
	s_ashr_i32 s5, s4, 31
	s_lshl_b32 s3, s0, 2
	v_lshl_add_u64 v[36:37], v[10:11], 0, s[8:9]
	s_lshl_b32 s39, s35, 5
	s_lshl_b64 s[8:9], s[4:5], 12
	v_readlane_b32 s12, v254, 6
	v_readlane_b32 s13, v254, 7
	v_add_u32_e32 v14, s3, v18
	v_lshl_add_u64 v[16:17], s[68:69], 0, v[12:13]
	s_mov_b64 s[0:1], 0x27400000
	s_add_u32 s8, s68, s8
	v_readlane_b32 s14, v254, 8
	v_readlane_b32 s15, v254, 9
	v_lshl_add_u64 v[26:27], v[16:17], 0, s[0:1]
	v_mov_b64_e32 v[16:17], 0x23000000
	v_ashrrev_i32_e32 v15, 31, v14
	s_addc_u32 s9, s69, s9
	s_lshl_b32 s10, s76, 2
	s_mul_hi_i32 s12, s4, 0x380
	s_mul_i32 s13, s4, 0x380
	v_lshl_add_u64 v[28:29], v[10:11], 1, v[16:17]
	v_lshlrev_b64 v[32:33], 13, v[14:15]
	v_lshlrev_b32_e32 v15, 3, v1
	s_bfe_i32 s15, s10, 0x1001e
	s_bfe_i32 s14, s10, 0x1f0000
	v_mov_b32_e32 v10, s13
	v_mov_b32_e32 v11, s12
	s_mov_b32 s12, 0x700000
	v_and_b32_e32 v34, 0x78, v15
	s_lshl_b64 s[10:11], s[14:15], 12
	v_mad_i64_i32 v[10:11], s[12:13], v14, s12, v[10:11]
	s_lshl_b64 s[16:17], s[4:5], 13
	v_or_b32_e32 v10, v10, v34
	s_add_u32 s16, s68, s16
	v_lshl_add_u64 v[10:11], s[68:69], 0, v[10:11]
	s_mov_b64 s[12:13], 0x3bc00200
	s_addc_u32 s17, s69, s17
	v_lshl_add_u64 v[40:41], v[10:11], 0, s[12:13]
	v_lshl_add_u64 v[10:11], s[16:17], 0, v[12:13]
	v_lshl_add_u64 v[30:31], s[68:69], 0, v[28:29]
	v_mov_b32_e32 v35, 0
	v_lshl_add_u64 v[38:39], s[68:69], 0, v[36:37]
	s_mul_i32 s40, s33, 3
	s_movk_i32 s41, 0x380
	s_mul_hi_i32 s13, s14, 0x380
	s_mul_i32 s12, s14, 0x380
	v_lshl_add_u64 v[42:43], v[10:11], 0, s[0:1]
	s_lshl_b64 s[14:15], s[14:15], 13
	v_mov_b32_e32 v68, 0x3a27c5ac
	s_mov_b32 s5, 0xf800000
	v_mov_b32_e32 v69, 0x260
	v_readlane_b32 s20, v254, 14
	v_readlane_b32 s21, v254, 15
	v_readlane_b32 s22, v254, 16
	v_readlane_b32 s23, v254, 17
	s_branch .LBB0_2883

; __device__ __forceinline__ void p6_rwkv_post(Frame& F) {
;     ...
;         for (int k = 0; k < 4; ++k) { const int t = tb + k * tstep; yy[k] = (f32x4){0.f, 0.f, 0.f, 0.f}; vv[k] = gg[k] = (v2u){0u, 0u}; bcv[k] = 0.f;
;             if (t < S_) { yy[k] = *(const f32x4*)(Y + (size_t)t * RW + c); vv[k] = *(const v2u*)(SC + ((size_t)h * S_ + t) * SCAN_REC + 512 + 8 * q); gg[k] = *(const v2u*)(GG + (size_t)t * RW + c); bcv[k] = BC[t * RH + h]; } }
.LBB0_2883:
	v_add_u32_e32 v10, s3, v45
	v_ashrrev_i32_e32 v11, 31, v10
	v_lshl_add_u64 v[10:11], v[10:11], 2, s[6:7]
	global_load_dword v64, v[10:11], off nt
	v_lshl_add_u64 v[10:11], s[8:9], 0, v[28:29]
	global_load_dwordx2 v[62:63], v[10:11], off nt
	global_load_dwordx2 v[66:67], v[40:41], off nt
	global_load_dwordx4 v[22:25], v[42:43], off nt
	s_add_i32 s18, s33, s4
	s_cmpk_lt_i32 s18, 0x2000
	s_cselect_b64 s[28:29], -1, 0
	s_cmpk_gt_i32 s18, 0x1fff
	s_cbranch_scc1 .LBB0_2885
	s_ashr_i32 s19, s18, 31
	s_lshl_b64 s[0:1], s[18:19], 13
	v_lshl_add_u64 v[12:13], v[32:33], 0, s[18:19]
	v_mov_b64_e32 v[14:15], s[68:69]
	v_lshl_add_u64 v[10:11], v[26:27], 0, s[0:1]
	v_mad_u64_u32 v[14:15], s[0:1], v12, s41, v[14:15]
	v_mad_i32_i24 v15, v13, s41, v15
	v_lshl_add_u64 v[12:13], v[14:15], 0, v[34:35]
	v_add_co_u32_e32 v12, vcc, 0x3bc00000, v12
	s_lshl_b64 s[0:1], s[18:19], 12
	s_nop 0
	v_addc_co_u32_e32 v13, vcc, 0, v13, vcc
	global_load_dwordx4 v[18:21], v[10:11], off nt
	global_load_dwordx2 v[60:61], v[12:13], off offset:512 nt
	v_add_u32_e32 v12, s3, v65
	v_lshl_add_u64 v[10:11], v[30:31], 0, s[0:1]
	v_ashrrev_i32_e32 v13, 31, v12
	v_lshl_add_u64 v[12:13], v[12:13], 2, s[6:7]
	global_load_dwordx2 v[52:53], v[10:11], off nt
	global_load_dword v58, v[12:13], off nt
	s_branch .LBB0_2886

; __device__ __forceinline__ void p6_rwkv_post(Frame& F) {
;     ...
;         for (int k = 0; k < 4; ++k) { const int t = tb + k * tstep; yy[k] = (f32x4){0.f, 0.f, 0.f, 0.f}; vv[k] = gg[k] = (v2u){0u, 0u}; bcv[k] = 0.f;
;             if (t < S_) { yy[k] = *(const f32x4*)(Y + (size_t)t * RW + c); vv[k] = *(const v2u*)(SC + ((size_t)h * S_ + t) * SCAN_REC + 512 + 8 * q); gg[k] = *(const v2u*)(GG + (size_t)t * RW + c); bcv[k] = BC[t * RH + h]; } }
.LBB0_2886:
	s_add_i32 s20, s38, s4
	s_cmpk_lt_i32 s20, 0x2000
	v_mov_b32_e32 v50, 0
	v_mov_b32_e32 v44, 0
	s_cselect_b64 s[30:31], -1, 0
	s_cmpk_gt_i32 s20, 0x1fff
	v_mov_b32_e32 v56, 0
	v_mov_b32_e32 v51, 0
	v_mov_b32_e32 v54, 0
	v_mov_b32_e32 v55, 0
	v_mov_b32_e32 v14, 0
	v_mov_b32_e32 v15, 0
	v_mov_b32_e32 v16, 0
	v_mov_b32_e32 v17, 0
	s_cbranch_scc1 .LBB0_2888
	s_ashr_i32 s21, s20, 31
	s_lshl_b64 s[0:1], s[20:21], 13
	v_lshl_add_u64 v[12:13], v[32:33], 0, s[20:21]
	v_mov_b64_e32 v[14:15], s[68:69]
	v_lshl_add_u64 v[10:11], v[26:27], 0, s[0:1]
	v_mad_u64_u32 v[14:15], s[0:1], v12, s41, v[14:15]
	v_mad_i32_i24 v15, v13, s41, v15
	v_lshl_add_u64 v[12:13], v[14:15], 0, v[34:35]
	v_add_co_u32_e32 v12, vcc, 0x3bc00000, v12
	s_lshl_b64 s[0:1], s[20:21], 12
	s_nop 0
	v_addc_co_u32_e32 v13, vcc, 0, v13, vcc
	global_load_dwordx4 v[14:17], v[10:11], off nt
	global_load_dwordx2 v[54:55], v[12:13], off offset:512 nt
	v_add_u32_e32 v12, s3, v57
	v_lshl_add_u64 v[10:11], v[30:31], 0, s[0:1]
	v_ashrrev_i32_e32 v13, 31, v12
	v_lshl_add_u64 v[12:13], v[12:13], 2, s[6:7]
	global_load_dwordx2 v[50:51], v[10:11], off nt
	global_load_dword v56, v[12:13], off nt
.LBB0_2888:
	s_add_i32 s16, s40, s4
	s_cmpk_lt_i32 s16, 0x2000
	s_cselect_b64 s[22:23], -1, 0
	s_cmpk_gt_i32 s16, 0x1fff
	v_mov_b32_e32 v46, 0
	v_mov_b32_e32 v47, 0
	v_mov_b32_e32 v48, 0
	v_mov_b32_e32 v49, 0
	v_mov_b32_e32 v10, 0
	v_mov_b32_e32 v11, 0
	v_mov_b32_e32 v12, 0
	v_mov_b32_e32 v13, 0
	s_cbranch_scc1 .LBB0_2890
	s_ashr_i32 s17, s16, 31
	s_lshl_b64 s[0:1], s[16:17], 13
	v_lshl_add_u64 v[12:13], v[32:33], 0, s[16:17]
	v_mov_b64_e32 v[46:47], s[68:69]
	v_lshl_add_u64 v[10:11], v[26:27], 0, s[0:1]
	v_mad_u64_u32 v[46:47], s[0:1], v12, s41, v[46:47]
	v_mad_i32_i24 v47, v13, s41, v47
	v_lshl_add_u64 v[12:13], v[46:47], 0, v[34:35]
	v_add_co_u32_e32 v46, vcc, 0x3bc00000, v12
	s_lshl_b64 s[0:1], s[16:17], 12
	s_nop 0
	v_addc_co_u32_e32 v47, vcc, 0, v13, vcc
	v_add_u32_e32 v70, s3, v59
	global_load_dwordx4 v[10:13], v[10:11], off nt
	s_nop 0
	global_load_dwordx2 v[48:49], v[46:47], off offset:512 nt
	v_lshl_add_u64 v[46:47], v[30:31], 0, s[0:1]
	v_ashrrev_i32_e32 v71, 31, v70
	v_lshl_add_u64 v[70:71], v[70:71], 2, s[6:7]
	global_load_dwordx2 v[46:47], v[46:47], off nt
	s_nop 0
	global_load_dword v44, v[70:71], off nt

; __device__ __forceinline__ void p6_moba_combine(Frame& F) {
;     const bf16* PO = (const bf16*)(F.ws + WS_PARTO); const float* PML = (const float*)(F.ws + WS_PARTML); bf16* YB = (bf16*)(F.ws + WS_YA);
;     for (int t = F.gw; t < S_; t += F.NGW) {
;         const int h = F.lane >> 2, dq = F.lane & 3, blk = t >> 8, nsel = blk < 3 ? blk : 3; const size_t base = (size_t)(t * MH + h) * 4;
;         const f32x4 ml0 = *(const f32x4*)(PML + base * 2), ml1 = *(const f32x4*)(PML + base * 2 + 4);
;         v4u x[4][4];
; #pragma unroll
;         for (int s = 0; s < 4; ++s)
; #pragma unroll
;             for (int k = 0; k < 4; ++k) x[s][k] = *(const v4u*)(PO + (base + s) * MD + dq * 32 + k * 8);
;         const float ms[4] = {ml0.x, ml0.z, ml1.x, ml1.z}, ls[4] = {ml0.y, ml0.w, ml1.y, ml1.w};
;         float M = ms[3];
; #pragma unroll
;         for (int s = 0; s < 3; ++s) if (s < nsel) M = fmaxf(M, ms[s]);
;         float wsum = 0.f, w[4];
; #pragma unroll
;         for (int s = 0; s < 4; ++s) { w[s] = (s == 3 || s < nsel) ? __expf(ms[s] - M) * ls[s] : 0.f; wsum += w[s]; }
.LBB0_2899:
	v_ashrrev_i32_e32 v75, 31, v74
	v_lshlrev_b64 v[2:3], 5, v[74:75]
	v_lshl_add_u64 v[2:3], s[12:13], 0, v[2:3]
	global_load_dwordx4 v[66:69], v[2:3], off nt
	global_load_dwordx4 v[54:57], v[2:3], off offset:16 nt
	v_lshlrev_b64 v[2:3], 10, v[74:75]
	v_lshl_add_u64 v[78:79], v[72:73], 0, v[2:3]
	global_load_dwordx4 v[30:33], v[78:79], off offset:32 nt
	global_load_dwordx4 v[46:49], v[78:79], off offset:16 nt
	global_load_dwordx4 v[26:29], v[78:79], off offset:288 nt
	global_load_dwordx4 v[42:45], v[78:79], off offset:272 nt
	global_load_dwordx4 v[14:17], v[78:79], off offset:48 nt
	global_load_dwordx4 v[62:65], v[78:79], off offset:256 nt
	global_load_dwordx4 v[22:25], v[78:79], off offset:544 nt
	global_load_dwordx4 v[38:41], v[78:79], off offset:528 nt
	global_load_dwordx4 v[10:13], v[78:79], off offset:304 nt
	global_load_dwordx4 v[58:61], v[78:79], off offset:512 nt
	global_load_dwordx4 v[2:5], v[78:79], off offset:816 nt
	global_load_dwordx4 v[18:21], v[78:79], off offset:800 nt
	global_load_dwordx4 v[34:37], v[78:79], off offset:784 nt
	global_load_dwordx4 v[6:9], v[78:79], off offset:560 nt
	global_load_dwordx4 v[50:53], v[78:79], off offset:768 nt
	s_ashr_i32 s0, s16, 8
	s_cmp_gt_i32 s0, 0
	s_cselect_b64 s[8:9], -1, 0
	s_cmp_gt_i32 s0, 1
	s_cselect_b64 s[10:11], -1, 0
	s_cmp_gt_i32 s0, 2
	s_cselect_b64 s[6:7], -1, 0
	s_cmp_lt_i32 s0, 1
	s_waitcnt vmcnt(16)
	v_max_f32_e32 v1, v66, v66
	s_waitcnt vmcnt(15)
	v_max_f32_e32 v71, v56, v56
	v_max_f32_e32 v1, v71, v1
	v_cndmask_b32_e64 v1, v56, v1, s[8:9]
	v_max_f32_e32 v75, v68, v68
	v_max_f32_e32 v71, v1, v1
	v_max_f32_e32 v71, v71, v75
	v_cndmask_b32_e64 v1, v1, v71, s[10:11]
	v_max_f32_e32 v80, v54, v54
	v_max_f32_e32 v71, v1, v1
	v_max_f32_e32 v75, v71, v80
	v_cndmask_b32_e64 v1, v1, v75, s[6:7]
	v_sub_f32_e32 v66, v66, v1
	v_mul_f32_e32 v66, 0x3fb8aa3b, v66
	v_exp_f32_e32 v66, v66
	s_nop 0
	v_mul_f32_e32 v66, v67, v66
	s_cbranch_scc1 .LBB0_2901
	global_load_dwordx4 v[78:81], v[78:79], off nt
	s_waitcnt vmcnt(0)
	v_lshlrev_b32_e32 v82, 16, v78
	v_and_b32_e32 v83, 0xffff0000, v78
	v_lshlrev_b32_e32 v78, 16, v79
	v_and_b32_e32 v79, 0xffff0000, v79
	v_lshlrev_b32_e32 v86, 16, v80
	v_and_b32_e32 v87, 0xffff0000, v80
	v_lshlrev_b32_e32 v88, 16, v81
	v_and_b32_e32 v89, 0xffff0000, v81
	v_pk_fma_f32 v[82:83], v[66:67], v[82:83], 0 op_sel_hi:[0,1,0]
	v_pk_fma_f32 v[84:85], v[66:67], v[78:79], 0 op_sel_hi:[0,1,0]
	v_pk_fma_f32 v[80:81], v[66:67], v[86:87], 0 op_sel_hi:[0,1,0]
	v_pk_fma_f32 v[78:79], v[66:67], v[88:89], 0 op_sel_hi:[0,1,0]
	s_branch .LBB0_2902
